# attention queues: each XCD group walks its four heads one at a time (K/V working set ~2.5 MB per L2) instead of two at a time
# speedup vs baseline: 1.0024x; 1.0024x over previous
; #define LAS __attribute__((address_space(3)))
; template <bool MLA>
; __device__ __forceinline__ void attn_unit(const P& p, LAS unsigned char* lds, const int b, const int h, const int qb) {
;     ...
;     const int tid = threadIdx.x, wid = __builtin_amdgcn_readfirstlane(tid >> 6), lane = tid & 63, r32 = lane & 31, hi = lane >> 5;
;     const int q0 = qb * 256, qw = q0 + 32 * wid, qi = qw + r32, nt = (q0 + 256) / 64;
;     const bf16_t* Kn = MLA ? WSP(bf16_t, WS_KNOPE) : WSP(bf16_t, WS_SBK);
;     const bf16_t* Kr = WSP(bf16_t, WS_KROPE);
;     const bf16_t* Vt = WSP(bf16_t, MLA ? WS_VMT : WS_SBVT) + (size_t)(b * 8 + h) * 128 * SEQ;
;     LAS float* al = (LAS float*)(lds + LDS_AL) + wid * 32;
;     LAS int* flag = (LAS int*)(lds + LDS_FLAG);
;     bf16x8 qf[NQF];
;     { const char* qb_ = MLA ? (const char*)WSP(bf16_t, WS_QMLA) + ((size_t)(b * SEQ + qw) * 1536 + h * 192) * 2 : (const char*)WSP(bf16_t, WS_SBQ) + ((size_t)(b * SEQ + qw) * 1024 + h * 128) * 2;
;       const unsigned qo = (unsigned)((r32 * (MLA ? 1536 : 1024) + 8 * hi) * 2);
; #pragma unroll
;       for (int s = 0; s < NQF; ++s) qf[s] = *(const bf16x8*)(qb_ + qo + 32 * s); }
;     bf16x8 tri0, tri1, ones;
; #pragma unroll
;     for (int j = 0; j < 8; ++j) { const int k0_ = 8 * (j >> 2) + 4 * hi + (j & 3); tri0[j] = (k0_ > r32) ? (short)0x3F80 : (short)0; tri1[j] = (16 + k0_ > r32) ? (short)0x3F80 : (short)0; ones[j] = (short)0x3F80; }
;     u32x4 kreg[NKR], vreg[2];
;     const unsigned kofs0 = (unsigned)(((tid >> 4) * 1024 + (tid & 15) * 8) * 2), kofs1 = kofs0 + 32u * 1024u * 2u;
;     const unsigned rofs = (unsigned)(((tid >> 3) * 64 + (tid & 7) * 8) * 2);
;     const unsigned vofs0 = (unsigned)(((tid >> 3) * SEQ + (tid & 7) * 8) * 2), vofs1 = vofs0 + 64u * SEQ * 2u;
;     const unsigned kw0 = (unsigned)((tid >> 4) * KSTR + (tid & 15) * 16), kw1 = kw0 + 32u * KSTR, rw = (unsigned)((tid >> 3) * KSTR + 256 + (tid & 7) * 16);
; __device__ __forceinline__ void attn_queues(const P& p, LAS unsigned char* lds, int* ctr, const int xg) {
;     ...
;         while (v < nq) {
;             __syncthreads();
;             if (tid == 0) qs[0] = atomicAdd(c0, 1);
;             const int bh = xg >= 0 ? xg * 4 + 2 * (v >> 5) + (v & 1) : (v & 31), qb = 15 - (xg >= 0 ? ((v & 31) >> 1) : (v >> 5));
;             attn_unit<true>(p, lds, bh >> 3, bh & 7, qb);
.LBB0_703:
	s_andn2_b64 vcc, exec, s[8:9]
	s_cbranch_vccnz .LBB0_705
	s_ashr_i32 s0, s2, 4
	s_and_b32 s0, s0, -1
	s_add_i32 s0, s0, s41
	s_mov_b32 s1, 0
	s_or_b32 s0, s0, s1
.LBB0_705:
	v_readlane_b32 s8, v242, 40
	s_and_b32 s1, s2, 15
	s_lshr_b32 s2, s2, 5
	v_readlane_b32 s9, v242, 41
	s_and_b64 s[8:9], s[8:9], exec
	s_cselect_b32 s1, s1, s2
	v_readfirstlane_b32 s2, v0
	s_lshl_b32 s13, s1, 8
	s_lshr_b32 s1, s2, 1
	s_and_b32 s14, s1, 0x7fffffe0
	s_sub_i32 s93, s14, s13
	s_ashr_i32 s1, s0, 31
	s_ashr_i32 s8, s0, 3
	s_and_b32 s12, s0, 7
	s_add_i32 s2, s93, 0xf00
	s_sub_i32 s9, 0x1000, s13
	s_lshl_b64 s[0:1], s[0:1], 20
	s_add_u32 s0, s88, s0
	s_addc_u32 s1, s89, s1
	s_lshl_b32 s10, s8, 12
	s_add_i32 s82, s2, s10
	s_mul_i32 s10, s82, 0x600
	s_mul_i32 s15, s12, 0xc0
	s_mul_hi_i32 s11, s82, 0x600
	s_or_b32 s10, s10, s15
	s_lshr_b32 s92, s9, 6
	s_ashr_i32 s9, s8, 31
	s_ashr_i32 s83, s82, 31
	v_lshl_add_u64 v[4:5], s[10:11], 1, v[188:189]
	s_lshl_b32 s90, s12, 7
	s_lshl_b64 s[10:11], s[8:9], 23
	s_add_u32 s10, s76, s10
	s_addc_u32 s11, s77, s11
	s_lshl_b32 s15, s14, 2
	s_add_i32 s91, s15, 0
	s_lshl_b64 s[8:9], s[8:9], 19
	s_add_i32 s91, s91, 0x16000
	s_lshl_b32 s12, s12, 8
	s_add_u32 s10, s10, s12
	s_addc_u32 s11, s11, 0
	global_load_dwordx4 v[114:117], v[4:5], off offset:32
	global_load_dwordx4 v[118:121], v[4:5], off offset:64
	global_load_dwordx4 v[122:125], v[4:5], off offset:96
	global_load_dwordx4 v[126:129], v[4:5], off offset:128
	v_lshl_add_u64 v[192:193], s[10:11], 0, v[182:183]
	s_mov_b32 s10, 0x10000
	v_add_co_u32_e32 v6, vcc, s10, v192
	v_lshl_add_u64 v[194:195], v[190:191], 0, s[8:9]
	s_nop 0
	v_addc_co_u32_e32 v7, vcc, 0, v193, vcc
	global_load_dwordx4 v[130:133], v[4:5], off offset:352
	global_load_dwordx4 v[142:145], v[6:7], off
	global_load_dwordx4 v[138:141], v[192:193], off
	global_load_dwordx4 v[170:173], v[194:195], off
	v_lshl_add_u64 v[196:197], s[0:1], 0, v[184:185]
	global_load_dwordx4 v[134:137], v[4:5], off
	global_load_dwordx4 v[174:177], v[196:197], off
	s_mov_b32 s0, 0x80000
	v_add_co_u32_e32 v6, vcc, s0, v196
	s_waitcnt vmcnt(10)
	v_mov_b32_e32 v16, v2
	v_addc_co_u32_e32 v7, vcc, 0, v197, vcc
	global_load_dwordx4 v[178:181], v[6:7], off
	global_load_dwordx4 v[146:149], v[4:5], off offset:160
	global_load_dwordx4 v[150:153], v[4:5], off offset:192
	global_load_dwordx4 v[154:157], v[4:5], off offset:224
	global_load_dwordx4 v[158:161], v[4:5], off offset:256
	global_load_dwordx4 v[162:165], v[4:5], off offset:288
	global_load_dwordx4 v[166:169], v[4:5], off offset:320
	v_mov_b32_e32 v17, v2
	v_add_u32_e32 v50, s14, v205
	v_mov_b32_e32 v3, v2
	v_mov_b32_e32 v4, v2
	v_mov_b32_e32 v5, v2
	v_mov_b32_e32 v6, v2
	v_mov_b32_e32 v7, v2
	v_mov_b32_e32 v8, v2
	v_mov_b32_e32 v9, v2
	v_mov_b32_e32 v10, v2
	v_mov_b32_e32 v11, v2
	v_mov_b32_e32 v12, v2
	v_mov_b32_e32 v13, v2
	v_mov_b32_e32 v14, v2
	v_mov_b32_e32 v15, v2
	v_mov_b64_e32 v[32:33], v[16:17]
	v_mov_b64_e32 v[48:49], v[16:17]
	v_subrev_u32_e32 v213, s13, v50
	v_mov_b64_e32 v[64:65], v[16:17]
	v_mov_b64_e32 v[80:81], v[16:17]
	s_mov_b32 s0, 0
	v_mov_b32_e32 v215, 0
	v_mov_b32_e32 v216, 0xf149f2ca
	s_mov_b32 s84, 64
	v_mov_b64_e32 v[30:31], v[14:15]
	v_mov_b64_e32 v[28:29], v[12:13]
	v_mov_b64_e32 v[26:27], v[10:11]
	v_mov_b64_e32 v[24:25], v[8:9]
	v_mov_b64_e32 v[22:23], v[6:7]
	v_mov_b64_e32 v[20:21], v[4:5]
	v_mov_b64_e32 v[18:19], v[2:3]
	v_mov_b64_e32 v[46:47], v[14:15]
	v_mov_b64_e32 v[44:45], v[12:13]
	v_mov_b64_e32 v[42:43], v[10:11]
	v_mov_b64_e32 v[40:41], v[8:9]
	v_mov_b64_e32 v[38:39], v[6:7]
	v_mov_b64_e32 v[36:37], v[4:5]
	v_mov_b64_e32 v[34:35], v[2:3]
	v_lshl_add_u32 v212, v1, 2, s91
	v_lshl_add_u32 v214, v203, 2, s91
	s_addk_i32 s93, 0xf1f
	v_mov_b64_e32 v[62:63], v[14:15]
	v_mov_b64_e32 v[60:61], v[12:13]
	v_mov_b64_e32 v[58:59], v[10:11]
	v_mov_b64_e32 v[56:57], v[8:9]
	v_mov_b64_e32 v[54:55], v[6:7]
	v_mov_b64_e32 v[52:53], v[4:5]
	v_mov_b64_e32 v[50:51], v[2:3]
	v_mov_b64_e32 v[78:79], v[14:15]
	v_mov_b64_e32 v[76:77], v[12:13]
	v_mov_b64_e32 v[74:75], v[10:11]
	v_mov_b64_e32 v[72:73], v[8:9]
	v_mov_b64_e32 v[70:71], v[6:7]
	v_mov_b64_e32 v[68:69], v[4:5]
	v_mov_b64_e32 v[66:67], v[2:3]
	s_waitcnt vmcnt(10)
	ds_write_b128 v206, v[138:141]
	ds_write_b128 v206, v[142:145] offset:12800
	s_waitcnt vmcnt(9)
	ds_write_b128 v207, v[170:173] offset:256
	s_waitcnt vmcnt(7)
	ds_write2_b64 v208, v[174:175], v[176:177] offset0:128 offset1:130
	s_waitcnt vmcnt(0)
	ds_write2_b64 v209, v[178:179], v[180:181] offset1:2
	s_waitcnt lgkmcnt(0)
	s_barrier

; #define LAS __attribute__((address_space(3)))
; template <bool MLA>
; __device__ __forceinline__ void attn_unit(const P& p, LAS unsigned char* lds, const int b, const int h, const int qb) {
;     ...
;     const int tid = threadIdx.x, wid = __builtin_amdgcn_readfirstlane(tid >> 6), lane = tid & 63, r32 = lane & 31, hi = lane >> 5;
;     const int q0 = qb * 256, qw = q0 + 32 * wid, qi = qw + r32, nt = (q0 + 256) / 64;
;     const bf16_t* Kn = MLA ? WSP(bf16_t, WS_KNOPE) : WSP(bf16_t, WS_SBK);
;     const bf16_t* Kr = WSP(bf16_t, WS_KROPE);
;     const bf16_t* Vt = WSP(bf16_t, MLA ? WS_VMT : WS_SBVT) + (size_t)(b * 8 + h) * 128 * SEQ;
;     LAS float* al = (LAS float*)(lds + LDS_AL) + wid * 32;
;     LAS int* flag = (LAS int*)(lds + LDS_FLAG);
;     bf16x8 qf[NQF];
;     { const char* qb_ = MLA ? (const char*)WSP(bf16_t, WS_QMLA) + ((size_t)(b * SEQ + qw) * 1536 + h * 192) * 2 : (const char*)WSP(bf16_t, WS_SBQ) + ((size_t)(b * SEQ + qw) * 1024 + h * 128) * 2;
;       const unsigned qo = (unsigned)((r32 * (MLA ? 1536 : 1024) + 8 * hi) * 2);
; #pragma unroll
;       for (int s = 0; s < NQF; ++s) qf[s] = *(const bf16x8*)(qb_ + qo + 32 * s); }
;     bf16x8 tri0, tri1, ones;
; #pragma unroll
;     for (int j = 0; j < 8; ++j) { const int k0_ = 8 * (j >> 2) + 4 * hi + (j & 3); tri0[j] = (k0_ > r32) ? (short)0x3F80 : (short)0; tri1[j] = (16 + k0_ > r32) ? (short)0x3F80 : (short)0; ones[j] = (short)0x3F80; }
;     u32x4 kreg[NKR], vreg[2];
;     const unsigned kofs0 = (unsigned)(((tid >> 4) * 1024 + (tid & 15) * 8) * 2), kofs1 = kofs0 + 32u * 1024u * 2u;
;     const unsigned rofs = (unsigned)(((tid >> 3) * 64 + (tid & 7) * 8) * 2);
;     const unsigned vofs0 = (unsigned)(((tid >> 3) * SEQ + (tid & 7) * 8) * 2), vofs1 = vofs0 + 64u * SEQ * 2u;
;     const unsigned kw0 = (unsigned)((tid >> 4) * KSTR + (tid & 15) * 16), kw1 = kw0 + 32u * KSTR, rw = (unsigned)((tid >> 3) * KSTR + 256 + (tid & 7) * 16);
; __device__ __forceinline__ void attn_queues(const P& p, LAS unsigned char* lds, int* ctr, const int xg) {
;     ...
;         while (v < nq) {
;             __syncthreads();
;             if (tid == 0) qs[0] = atomicAdd(c1, 1);
;             const int bh = xg >= 0 ? xg * 4 + 2 * (v >> 5) + (v & 1) : (v & 31), qb = 15 - (xg >= 0 ? ((v & 31) >> 1) : (v >> 5));
;             attn_unit<false>(p, lds, bh >> 3, bh & 7, qb);
.LBB0_736:
	s_andn2_b64 vcc, exec, s[10:11]
	s_cbranch_vccnz .LBB0_738
	s_ashr_i32 s0, s2, 4
	s_and_b32 s0, s0, -1
	v_readlane_b32 s1, v242, 48
	s_add_i32 s0, s0, s1
	s_mov_b32 s1, 0
	s_or_b32 s0, s0, s1
.LBB0_738:
	v_readlane_b32 s10, v242, 40
	s_and_b32 s1, s2, 15
	s_lshr_b32 s2, s2, 5
	v_readlane_b32 s11, v242, 41
	s_and_b64 s[10:11], s[10:11], exec
	s_cselect_b32 s1, s1, s2
	v_readfirstlane_b32 s2, v0
	s_lshr_b32 s14, s2, 6
	s_lshl_b32 s15, s1, 8
	s_lshl_b32 s16, s14, 5
	s_ashr_i32 s10, s0, 3
	s_sub_i32 s2, s16, s15
	s_addk_i32 s2, 0xf00
	s_lshl_b32 s1, s10, 12
	s_add_i32 s96, s2, s1
	s_lshl_b32 s1, s0, 7
	s_ashr_i32 s97, s96, 31
	s_and_b32 s1, s1, 0x380
	s_lshl_b64 s[12:13], s[96:97], 11
	s_lshl_b32 s33, s1, 1
	v_readlane_b32 s1, v242, 55
	s_add_u32 s1, s1, s12
	v_readlane_b32 s11, v242, 57
	s_addc_u32 s11, s11, s13
	s_add_u32 s12, s1, s33
	s_addc_u32 s13, s11, 0
	v_lshl_add_u64 v[4:5], s[12:13], 0, v[170:171]
	global_load_dwordx4 v[122:125], v[4:5], off
	global_load_dwordx4 v[126:129], v[4:5], off offset:32
	global_load_dwordx4 v[130:133], v[4:5], off offset:64
	global_load_dwordx4 v[134:137], v[4:5], off offset:96
	global_load_dwordx4 v[138:141], v[4:5], off offset:128
	global_load_dwordx4 v[142:145], v[4:5], off offset:160
	global_load_dwordx4 v[146:149], v[4:5], off offset:192
	global_load_dwordx4 v[150:153], v[4:5], off offset:224
	s_mov_b64 s[12:13], exec
	v_readlane_b32 s18, v242, 49
	v_readlane_b32 s19, v242, 50
	s_and_b64 s[18:19], s[12:13], s[18:19]
	s_mov_b64 exec, s[18:19]
	ds_write_b32 v183, v2
	s_or_b64 exec, exec, s[12:13]
	s_sub_i32 s17, 0x1000, s15
	s_ashr_i32 s1, s0, 31
	s_ashr_i32 s11, s10, 31
	s_lshl_b64 s[0:1], s[0:1], 20
	s_lshr_b32 s41, s17, 6
	s_lshl_b64 s[10:11], s[10:11], 23
	v_readlane_b32 s12, v242, 51
	s_add_u32 s12, s12, s10
	v_readlane_b32 s10, v242, 53
	s_addc_u32 s13, s10, s11
	v_readlane_b32 s10, v242, 59
	s_add_u32 s10, s10, s0
	v_readlane_b32 s0, v242, 60
	s_addc_u32 s11, s0, s1
	s_add_u32 s12, s12, s33
	s_addc_u32 s13, s13, 0
	s_andn2_b32 s17, s17, 63
	s_sub_i32 s94, s17, 64
	s_lshl_b64 s[0:1], s[94:95], 11
	s_add_u32 s0, s12, s0
	s_addc_u32 s1, s13, s1
	s_lshl_b64 s[18:19], s[94:95], 1
	s_add_u32 s18, s10, s18
	v_lshl_add_u64 v[4:5], s[0:1], 0, v[172:173]
	s_addc_u32 s19, s11, s19
	v_add_co_u32_e32 v6, vcc, s20, v4
	s_mov_b32 s0, 0x80000
	s_nop 0
	v_addc_co_u32_e32 v7, vcc, 0, v5, vcc
	global_load_dwordx4 v[154:157], v[4:5], off
	global_load_dwordx4 v[158:161], v[6:7], off
	v_lshl_add_u64 v[4:5], s[18:19], 0, v[174:175]
	v_add_co_u32_e32 v6, vcc, s0, v4
	v_add_u32_e32 v18, 0, v184
	s_nop 0
	v_addc_co_u32_e32 v7, vcc, 0, v5, vcc
	global_load_dwordx4 v[162:165], v[4:5], off
	global_load_dwordx4 v[166:169], v[6:7], off
	v_add_u32_e32 v50, 0, v182
	v_mov_b32_e32 v16, v2
	v_mov_b32_e32 v17, v2
	v_add_u32_e32 v51, 0x4000, v18
	v_add_u32_e32 v52, 0x6800, v18
	s_lshl_b32 s1, s14, 2
	v_mov_b32_e32 v3, v2
	v_mov_b32_e32 v4, v2
	v_mov_b32_e32 v5, v2
	v_mov_b32_e32 v6, v2
	v_mov_b32_e32 v7, v2
	v_mov_b32_e32 v8, v2
	v_mov_b32_e32 v9, v2
	v_mov_b32_e32 v10, v2
	v_mov_b32_e32 v11, v2
	v_mov_b32_e32 v12, v2
	v_mov_b32_e32 v13, v2
	v_mov_b32_e32 v14, v2
	v_mov_b32_e32 v15, v2
	v_mov_b64_e32 v[80:81], v[16:17]
	v_mov_b64_e32 v[48:49], v[16:17]
	v_mov_b64_e32 v[32:33], v[16:17]
	s_add_i32 s92, s1, 0
	s_mov_b32 s0, 0
	v_add_u32_e32 v190, s16, v187
	v_mov_b32_e32 v191, 0
	v_mov_b64_e32 v[78:79], v[14:15]
	v_mov_b64_e32 v[76:77], v[12:13]
	v_mov_b64_e32 v[74:75], v[10:11]
	v_mov_b64_e32 v[72:73], v[8:9]
	v_mov_b64_e32 v[70:71], v[6:7]
	v_mov_b64_e32 v[68:69], v[4:5]
	v_mov_b64_e32 v[66:67], v[2:3]
	v_mov_b64_e32 v[46:47], v[14:15]
	v_mov_b64_e32 v[44:45], v[12:13]
	v_mov_b64_e32 v[42:43], v[10:11]
	v_mov_b64_e32 v[40:41], v[8:9]
	v_mov_b64_e32 v[38:39], v[6:7]
	v_mov_b64_e32 v[36:37], v[4:5]
	v_mov_b64_e32 v[34:35], v[2:3]
	v_mov_b64_e32 v[30:31], v[14:15]
	v_mov_b64_e32 v[28:29], v[12:13]
	v_mov_b64_e32 v[26:27], v[10:11]
	v_mov_b64_e32 v[24:25], v[8:9]
	v_mov_b64_e32 v[22:23], v[6:7]
	v_mov_b64_e32 v[20:21], v[4:5]
	v_mov_b64_e32 v[18:19], v[2:3]
	v_lshl_add_u64 v[178:179], s[10:11], 0, v[174:175]
	v_lshl_add_u64 v[180:181], s[12:13], 0, v[172:173]
	s_or_b32 s94, s2, 31
	s_sub_i32 s93, 0xfff, s15
	s_add_i32 s92, s92, 0x16400
	s_waitcnt vmcnt(3)
	ds_write_b128 v50, v[154:157]
	s_waitcnt vmcnt(2)
	ds_write_b128 v50, v[158:161] offset:8704
	s_waitcnt vmcnt(1)
	ds_write2_b64 v51, v[162:163], v[164:165] offset0:128 offset1:130
	s_waitcnt vmcnt(0)
	ds_write2_b64 v52, v[166:167], v[168:169] offset1:2
	v_mov_b64_e32 v[64:65], v[16:17]
	v_mov_b64_e32 v[62:63], v[14:15]
	v_mov_b64_e32 v[60:61], v[12:13]
	v_mov_b64_e32 v[58:59], v[10:11]
	v_mov_b64_e32 v[56:57], v[8:9]
	v_mov_b64_e32 v[54:55], v[6:7]
	v_mov_b64_e32 v[52:53], v[4:5]
	v_mov_b64_e32 v[50:51], v[2:3]
	s_waitcnt lgkmcnt(0)
	s_barrier
	s_cmp_eq_u32 s41, s0
	s_cbranch_scc0 .LBB0_742

; #define LAS __attribute__((address_space(3)))
; template <bool MLA>
; __device__ __forceinline__ void attn_unit(const P& p, LAS unsigned char* lds, const int b, const int h, const int qb) {
;     ...
;     const int tid = threadIdx.x, wid = __builtin_amdgcn_readfirstlane(tid >> 6), lane = tid & 63, r32 = lane & 31, hi = lane >> 5;
;     const int q0 = qb * 256, qw = q0 + 32 * wid, qi = qw + r32, nt = (q0 + 256) / 64;
;     const bf16_t* Kn = MLA ? WSP(bf16_t, WS_KNOPE) : WSP(bf16_t, WS_SBK);
;     const bf16_t* Kr = WSP(bf16_t, WS_KROPE);
;     const bf16_t* Vt = WSP(bf16_t, MLA ? WS_VMT : WS_SBVT) + (size_t)(b * 8 + h) * 128 * SEQ;
;     LAS float* al = (LAS float*)(lds + LDS_AL) + wid * 32;
;     LAS int* flag = (LAS int*)(lds + LDS_FLAG);
;     bf16x8 qf[NQF];
;     { const char* qb_ = MLA ? (const char*)WSP(bf16_t, WS_QMLA) + ((size_t)(b * SEQ + qw) * 1536 + h * 192) * 2 : (const char*)WSP(bf16_t, WS_SBQ) + ((size_t)(b * SEQ + qw) * 1024 + h * 128) * 2;
;       const unsigned qo = (unsigned)((r32 * (MLA ? 1536 : 1024) + 8 * hi) * 2);
; #pragma unroll
;       for (int s = 0; s < NQF; ++s) qf[s] = *(const bf16x8*)(qb_ + qo + 32 * s); }
;     bf16x8 tri0, tri1, ones;
; #pragma unroll
;     for (int j = 0; j < 8; ++j) { const int k0_ = 8 * (j >> 2) + 4 * hi + (j & 3); tri0[j] = (k0_ > r32) ? (short)0x3F80 : (short)0; tri1[j] = (16 + k0_ > r32) ? (short)0x3F80 : (short)0; ones[j] = (short)0x3F80; }
;     u32x4 kreg[NKR], vreg[2];
;     const unsigned kofs0 = (unsigned)(((tid >> 4) * 1024 + (tid & 15) * 8) * 2), kofs1 = kofs0 + 32u * 1024u * 2u;
;     const unsigned rofs = (unsigned)(((tid >> 3) * 64 + (tid & 7) * 8) * 2);
;     const unsigned vofs0 = (unsigned)(((tid >> 3) * SEQ + (tid & 7) * 8) * 2), vofs1 = vofs0 + 64u * SEQ * 2u;
;     const unsigned kw0 = (unsigned)((tid >> 4) * KSTR + (tid & 15) * 16), kw1 = kw0 + 32u * KSTR, rw = (unsigned)((tid >> 3) * KSTR + 256 + (tid & 7) * 16);
; __device__ __forceinline__ void attn_queues(const P& p, LAS unsigned char* lds, int* ctr, const int xg) {
;     ...
;         while (v < nq) {
;             __syncthreads();
;             if (tid == 0) qs[0] = atomicAdd(c0, 1);
;             const int bh = xg >= 0 ? xg * 4 + 2 * (v >> 5) + (v & 1) : (v & 31), qb = 15 - (xg >= 0 ? ((v & 31) >> 1) : (v >> 5));
;             attn_unit<true>(p, lds, bh >> 3, bh & 7, qb);
.LBB0_871:
	v_readlane_b32 s8, v242, 40
	s_and_b32 s1, s2, 15
	s_lshr_b32 s2, s2, 5
	v_readlane_b32 s9, v242, 41
	s_and_b64 s[8:9], s[8:9], exec
	s_cselect_b32 s1, s1, s2
	v_readfirstlane_b32 s2, v0
	s_lshl_b32 s13, s1, 8
	s_lshr_b32 s1, s2, 1
	s_and_b32 s14, s1, 0x7fffffe0
	s_sub_i32 s93, s14, s13
	s_ashr_i32 s1, s0, 31
	s_ashr_i32 s8, s0, 3
	s_and_b32 s12, s0, 7
	s_add_i32 s2, s93, 0xf00
	s_sub_i32 s9, 0x1000, s13
	s_lshl_b64 s[0:1], s[0:1], 20
	s_add_u32 s0, s88, s0
	s_addc_u32 s1, s89, s1
	s_lshl_b32 s10, s8, 12
	s_add_i32 s82, s2, s10
	s_mul_i32 s10, s82, 0x600
	s_mul_i32 s15, s12, 0xc0
	s_mul_hi_i32 s11, s82, 0x600
	s_or_b32 s10, s10, s15
	s_lshr_b32 s92, s9, 6
	s_ashr_i32 s9, s8, 31
	s_ashr_i32 s83, s82, 31
	v_lshl_add_u64 v[4:5], s[10:11], 1, v[188:189]
	s_lshl_b32 s90, s12, 7
	s_lshl_b64 s[10:11], s[8:9], 23
	s_add_u32 s10, s76, s10
	s_addc_u32 s11, s77, s11
	s_lshl_b32 s15, s14, 2
	s_add_i32 s91, s15, 0
	s_lshl_b64 s[8:9], s[8:9], 19
	s_add_i32 s91, s91, 0x16000
	s_lshl_b32 s12, s12, 8
	s_add_u32 s10, s10, s12
	s_addc_u32 s11, s11, 0
	global_load_dwordx4 v[114:117], v[4:5], off offset:32
	global_load_dwordx4 v[118:121], v[4:5], off offset:64
	global_load_dwordx4 v[122:125], v[4:5], off offset:96
	global_load_dwordx4 v[126:129], v[4:5], off offset:128
	v_lshl_add_u64 v[192:193], s[10:11], 0, v[182:183]
	s_mov_b32 s10, 0x10000
	v_add_co_u32_e32 v6, vcc, s10, v192
	v_lshl_add_u64 v[194:195], v[190:191], 0, s[8:9]
	s_nop 0
	v_addc_co_u32_e32 v7, vcc, 0, v193, vcc
	global_load_dwordx4 v[130:133], v[4:5], off offset:352
	global_load_dwordx4 v[142:145], v[6:7], off
	global_load_dwordx4 v[138:141], v[192:193], off
	global_load_dwordx4 v[170:173], v[194:195], off
	v_lshl_add_u64 v[196:197], s[0:1], 0, v[184:185]
	global_load_dwordx4 v[134:137], v[4:5], off
	global_load_dwordx4 v[174:177], v[196:197], off
	s_mov_b32 s0, 0x80000
	v_add_co_u32_e32 v6, vcc, s0, v196
	s_waitcnt vmcnt(10)
	v_mov_b32_e32 v16, v2
	v_addc_co_u32_e32 v7, vcc, 0, v197, vcc
	global_load_dwordx4 v[178:181], v[6:7], off
	global_load_dwordx4 v[146:149], v[4:5], off offset:160
	global_load_dwordx4 v[150:153], v[4:5], off offset:192
	global_load_dwordx4 v[154:157], v[4:5], off offset:224
	global_load_dwordx4 v[158:161], v[4:5], off offset:256
	global_load_dwordx4 v[162:165], v[4:5], off offset:288
	global_load_dwordx4 v[166:169], v[4:5], off offset:320
	v_mov_b32_e32 v17, v2
	v_add_u32_e32 v50, s14, v208
	v_mov_b32_e32 v3, v2
	v_mov_b32_e32 v4, v2
	v_mov_b32_e32 v5, v2
	v_mov_b32_e32 v6, v2
	v_mov_b32_e32 v7, v2
	v_mov_b32_e32 v8, v2
	v_mov_b32_e32 v9, v2
	v_mov_b32_e32 v10, v2
	v_mov_b32_e32 v11, v2
	v_mov_b32_e32 v12, v2
	v_mov_b32_e32 v13, v2
	v_mov_b32_e32 v14, v2
	v_mov_b32_e32 v15, v2
	v_mov_b64_e32 v[32:33], v[16:17]
	v_mov_b64_e32 v[48:49], v[16:17]
	v_subrev_u32_e32 v216, s13, v50
	v_mov_b64_e32 v[64:65], v[16:17]
	v_mov_b64_e32 v[80:81], v[16:17]
	s_mov_b32 s0, 0
	v_mov_b32_e32 v218, 0
	v_mov_b32_e32 v219, 0xf149f2ca
	s_mov_b32 s84, 64
	v_mov_b64_e32 v[30:31], v[14:15]
	v_mov_b64_e32 v[28:29], v[12:13]
	v_mov_b64_e32 v[26:27], v[10:11]
	v_mov_b64_e32 v[24:25], v[8:9]
	v_mov_b64_e32 v[22:23], v[6:7]
	v_mov_b64_e32 v[20:21], v[4:5]
	v_mov_b64_e32 v[18:19], v[2:3]
	v_mov_b64_e32 v[46:47], v[14:15]
	v_mov_b64_e32 v[44:45], v[12:13]
	v_mov_b64_e32 v[42:43], v[10:11]
	v_mov_b64_e32 v[40:41], v[8:9]
	v_mov_b64_e32 v[38:39], v[6:7]
	v_mov_b64_e32 v[36:37], v[4:5]
	v_mov_b64_e32 v[34:35], v[2:3]
	v_lshl_add_u32 v215, v1, 2, s91
	v_lshl_add_u32 v217, v206, 2, s91
	s_addk_i32 s93, 0xf1f
	v_mov_b64_e32 v[62:63], v[14:15]
	v_mov_b64_e32 v[60:61], v[12:13]
	v_mov_b64_e32 v[58:59], v[10:11]
	v_mov_b64_e32 v[56:57], v[8:9]
	v_mov_b64_e32 v[54:55], v[6:7]
	v_mov_b64_e32 v[52:53], v[4:5]
	v_mov_b64_e32 v[50:51], v[2:3]
	v_mov_b64_e32 v[78:79], v[14:15]
	v_mov_b64_e32 v[76:77], v[12:13]
	v_mov_b64_e32 v[74:75], v[10:11]
	v_mov_b64_e32 v[72:73], v[8:9]
	v_mov_b64_e32 v[70:71], v[6:7]
	v_mov_b64_e32 v[68:69], v[4:5]
	v_mov_b64_e32 v[66:67], v[2:3]
	s_waitcnt vmcnt(10)
	ds_write_b128 v209, v[138:141]
	ds_write_b128 v209, v[142:145] offset:12800
	s_waitcnt vmcnt(9)
	ds_write_b128 v210, v[170:173] offset:256
	s_waitcnt vmcnt(7)
	ds_write2_b64 v211, v[174:175], v[176:177] offset0:128 offset1:130
	s_waitcnt vmcnt(0)
	ds_write2_b64 v212, v[178:179], v[180:181] offset1:2
	s_waitcnt lgkmcnt(0)
	s_barrier

; #define LAS __attribute__((address_space(3)))
; template <bool MLA>
; __device__ __forceinline__ void attn_unit(const P& p, LAS unsigned char* lds, const int b, const int h, const int qb) {
;     ...
;     const int tid = threadIdx.x, wid = __builtin_amdgcn_readfirstlane(tid >> 6), lane = tid & 63, r32 = lane & 31, hi = lane >> 5;
;     const int q0 = qb * 256, qw = q0 + 32 * wid, qi = qw + r32, nt = (q0 + 256) / 64;
;     const bf16_t* Kn = MLA ? WSP(bf16_t, WS_KNOPE) : WSP(bf16_t, WS_SBK);
;     const bf16_t* Kr = WSP(bf16_t, WS_KROPE);
;     const bf16_t* Vt = WSP(bf16_t, MLA ? WS_VMT : WS_SBVT) + (size_t)(b * 8 + h) * 128 * SEQ;
;     LAS float* al = (LAS float*)(lds + LDS_AL) + wid * 32;
;     LAS int* flag = (LAS int*)(lds + LDS_FLAG);
;     bf16x8 qf[NQF];
;     { const char* qb_ = MLA ? (const char*)WSP(bf16_t, WS_QMLA) + ((size_t)(b * SEQ + qw) * 1536 + h * 192) * 2 : (const char*)WSP(bf16_t, WS_SBQ) + ((size_t)(b * SEQ + qw) * 1024 + h * 128) * 2;
;       const unsigned qo = (unsigned)((r32 * (MLA ? 1536 : 1024) + 8 * hi) * 2);
; #pragma unroll
;       for (int s = 0; s < NQF; ++s) qf[s] = *(const bf16x8*)(qb_ + qo + 32 * s); }
;     bf16x8 tri0, tri1, ones;
; #pragma unroll
;     for (int j = 0; j < 8; ++j) { const int k0_ = 8 * (j >> 2) + 4 * hi + (j & 3); tri0[j] = (k0_ > r32) ? (short)0x3F80 : (short)0; tri1[j] = (16 + k0_ > r32) ? (short)0x3F80 : (short)0; ones[j] = (short)0x3F80; }
;     u32x4 kreg[NKR], vreg[2];
;     const unsigned kofs0 = (unsigned)(((tid >> 4) * 1024 + (tid & 15) * 8) * 2), kofs1 = kofs0 + 32u * 1024u * 2u;
;     const unsigned rofs = (unsigned)(((tid >> 3) * 64 + (tid & 7) * 8) * 2);
;     const unsigned vofs0 = (unsigned)(((tid >> 3) * SEQ + (tid & 7) * 8) * 2), vofs1 = vofs0 + 64u * SEQ * 2u;
;     const unsigned kw0 = (unsigned)((tid >> 4) * KSTR + (tid & 15) * 16), kw1 = kw0 + 32u * KSTR, rw = (unsigned)((tid >> 3) * KSTR + 256 + (tid & 7) * 16);
; __device__ __forceinline__ void attn_queues(const P& p, LAS unsigned char* lds, int* ctr, const int xg) {
;     ...
;         while (v < nq) {
;             __syncthreads();
;             if (tid == 0) qs[0] = atomicAdd(c1, 1);
;             const int bh = xg >= 0 ? xg * 4 + 2 * (v >> 5) + (v & 1) : (v & 31), qb = 15 - (xg >= 0 ? ((v & 31) >> 1) : (v >> 5));
;             attn_unit<false>(p, lds, bh >> 3, bh & 7, qb);
.LBB0_904:
	v_readlane_b32 s10, v242, 40
	s_and_b32 s1, s2, 15
	s_lshr_b32 s2, s2, 5
	v_readlane_b32 s11, v242, 41
	s_and_b64 s[10:11], s[10:11], exec
	s_cselect_b32 s1, s1, s2
	v_readfirstlane_b32 s2, v0
	s_lshr_b32 s14, s2, 6
	s_lshl_b32 s15, s1, 8
	s_lshl_b32 s16, s14, 5
	s_ashr_i32 s10, s0, 3
	s_sub_i32 s33, s16, s15
	s_addk_i32 s33, 0xf00
	s_lshl_b32 s1, s10, 12
	s_add_i32 s96, s33, s1
	s_lshl_b32 s1, s0, 7
	s_ashr_i32 s97, s96, 31
	s_and_b32 s1, s1, 0x380
	s_lshl_b64 s[12:13], s[96:97], 11
	s_lshl_b32 s2, s1, 1
	v_readlane_b32 s1, v242, 55
	s_add_u32 s1, s1, s12
	v_readlane_b32 s11, v242, 57
	s_addc_u32 s11, s11, s13
	s_add_u32 s12, s1, s2
	s_addc_u32 s13, s11, 0
	v_lshl_add_u64 v[4:5], s[12:13], 0, v[170:171]
	global_load_dwordx4 v[122:125], v[4:5], off
	global_load_dwordx4 v[126:129], v[4:5], off offset:32
	global_load_dwordx4 v[130:133], v[4:5], off offset:64
	global_load_dwordx4 v[134:137], v[4:5], off offset:96
	global_load_dwordx4 v[138:141], v[4:5], off offset:128
	global_load_dwordx4 v[142:145], v[4:5], off offset:160
	global_load_dwordx4 v[146:149], v[4:5], off offset:192
	global_load_dwordx4 v[150:153], v[4:5], off offset:224
	s_mov_b64 s[12:13], exec
	v_readlane_b32 s18, v242, 49
	v_readlane_b32 s19, v242, 50
	s_and_b64 s[18:19], s[12:13], s[18:19]
	s_mov_b64 exec, s[18:19]
	ds_write_b32 v183, v2
	s_or_b64 exec, exec, s[12:13]
	s_sub_i32 s17, 0x1000, s15
	s_ashr_i32 s1, s0, 31
	s_ashr_i32 s11, s10, 31
	s_lshl_b64 s[0:1], s[0:1], 20
	s_lshr_b32 s41, s17, 6
	s_lshl_b64 s[10:11], s[10:11], 23
	v_readlane_b32 s12, v242, 51
	s_add_u32 s12, s12, s10
	v_readlane_b32 s10, v242, 53
	s_addc_u32 s13, s10, s11
	v_readlane_b32 s10, v242, 59
	s_add_u32 s10, s10, s0
	v_readlane_b32 s0, v242, 60
	s_addc_u32 s11, s0, s1
	s_add_u32 s12, s12, s2
	s_addc_u32 s13, s13, 0
	s_andn2_b32 s17, s17, 63
	s_sub_i32 s94, s17, 64
	s_lshl_b64 s[0:1], s[94:95], 11
	s_add_u32 s0, s12, s0
	s_addc_u32 s1, s13, s1
	s_lshl_b64 s[18:19], s[94:95], 1
	s_add_u32 s18, s10, s18
	v_lshl_add_u64 v[4:5], s[0:1], 0, v[172:173]
	s_addc_u32 s19, s11, s19
	v_add_co_u32_e32 v6, vcc, s20, v4
	s_mov_b32 s0, 0x80000
	s_nop 0
	v_addc_co_u32_e32 v7, vcc, 0, v5, vcc
	global_load_dwordx4 v[154:157], v[4:5], off
	global_load_dwordx4 v[158:161], v[6:7], off
	v_lshl_add_u64 v[4:5], s[18:19], 0, v[174:175]
	v_add_co_u32_e32 v6, vcc, s0, v4
	v_add_u32_e32 v18, 0, v184
	s_nop 0
	v_addc_co_u32_e32 v7, vcc, 0, v5, vcc
	global_load_dwordx4 v[162:165], v[4:5], off
	global_load_dwordx4 v[166:169], v[6:7], off
	v_add_u32_e32 v50, 0, v182
	v_mov_b32_e32 v16, v2
	v_mov_b32_e32 v17, v2
	v_add_u32_e32 v51, 0x4000, v18
	v_add_u32_e32 v52, 0x6800, v18
	s_lshl_b32 s1, s14, 2
	v_mov_b32_e32 v3, v2
	v_mov_b32_e32 v4, v2
	v_mov_b32_e32 v5, v2
	v_mov_b32_e32 v6, v2
	v_mov_b32_e32 v7, v2
	v_mov_b32_e32 v8, v2
	v_mov_b32_e32 v9, v2
	v_mov_b32_e32 v10, v2
	v_mov_b32_e32 v11, v2
	v_mov_b32_e32 v12, v2
	v_mov_b32_e32 v13, v2
	v_mov_b32_e32 v14, v2
	v_mov_b32_e32 v15, v2
	v_mov_b64_e32 v[80:81], v[16:17]
	v_mov_b64_e32 v[48:49], v[16:17]
	v_mov_b64_e32 v[32:33], v[16:17]
	s_add_i32 s92, s1, 0
	s_mov_b32 s0, 0
	v_add_u32_e32 v190, s16, v187
	v_mov_b32_e32 v191, 0
	v_mov_b64_e32 v[78:79], v[14:15]
	v_mov_b64_e32 v[76:77], v[12:13]
	v_mov_b64_e32 v[74:75], v[10:11]
	v_mov_b64_e32 v[72:73], v[8:9]
	v_mov_b64_e32 v[70:71], v[6:7]
	v_mov_b64_e32 v[68:69], v[4:5]
	v_mov_b64_e32 v[66:67], v[2:3]
	v_mov_b64_e32 v[46:47], v[14:15]
	v_mov_b64_e32 v[44:45], v[12:13]
	v_mov_b64_e32 v[42:43], v[10:11]
	v_mov_b64_e32 v[40:41], v[8:9]
	v_mov_b64_e32 v[38:39], v[6:7]
	v_mov_b64_e32 v[36:37], v[4:5]
	v_mov_b64_e32 v[34:35], v[2:3]
	v_mov_b64_e32 v[30:31], v[14:15]
	v_mov_b64_e32 v[28:29], v[12:13]
	v_mov_b64_e32 v[26:27], v[10:11]
	v_mov_b64_e32 v[24:25], v[8:9]
	v_mov_b64_e32 v[22:23], v[6:7]
	v_mov_b64_e32 v[20:21], v[4:5]
	v_mov_b64_e32 v[18:19], v[2:3]
	v_lshl_add_u64 v[178:179], s[10:11], 0, v[174:175]
	v_lshl_add_u64 v[180:181], s[12:13], 0, v[172:173]
	s_or_b32 s94, s33, 31
	s_sub_i32 s93, 0xfff, s15
	s_add_i32 s92, s92, 0x16400
	s_waitcnt vmcnt(3)
	ds_write_b128 v50, v[154:157]
	s_waitcnt vmcnt(2)
	ds_write_b128 v50, v[158:161] offset:8704
	s_waitcnt vmcnt(1)
	ds_write2_b64 v51, v[162:163], v[164:165] offset0:128 offset1:130
	s_waitcnt vmcnt(0)
	ds_write2_b64 v52, v[166:167], v[168:169] offset1:2
	v_mov_b64_e32 v[64:65], v[16:17]
	v_mov_b64_e32 v[62:63], v[14:15]
	v_mov_b64_e32 v[60:61], v[12:13]
	v_mov_b64_e32 v[58:59], v[10:11]
	v_mov_b64_e32 v[56:57], v[8:9]
	v_mov_b64_e32 v[54:55], v[6:7]
	v_mov_b64_e32 v[52:53], v[4:5]
	v_mov_b64_e32 v[50:51], v[2:3]
	s_waitcnt lgkmcnt(0)
	s_barrier
	s_cmp_eq_u32 s41, s0
	s_cbranch_scc0 .LBB0_908
